# speedup vs baseline: 1.0091x; 1.0091x over previous
_Z10fin_kernelPKfS0_Pf:
	s_load_dwordx4 s[4:7], s[0:1], 0x0
	s_load_dwordx2 s[8:9], s[0:1], 0x10
	s_lshl_b32 s3, s2, 1
	s_mul_i32 s0, s2, 0x8b20
	s_mul_hi_i32 s1, s3, 0x4590
	s_lshl_b32 s10, s2, 14
	v_mov_b32_e32 v50, 0
	s_waitcnt lgkmcnt(0)
	s_add_u32 s10, s8, s10
	s_addc_u32 s11, s9, 0
	global_load_dword v50, v50, s[10:11]
	s_add_u32 s0, s4, s0
	s_addc_u32 s1, s5, s1
	v_lshlrev_b32_e32 v1, 5, v0
	global_load_dwordx4 v[2:5], v1, s[0:1]
	global_load_dwordx4 v[6:9], v1, s[0:1] offset:16
	s_or_b32 s0, s3, 1
	s_mul_hi_i32 s1, s0, 0x4590
	s_mulk_i32 s0, 0x4590
	s_add_u32 s0, s4, s0
	s_addc_u32 s1, s5, s1
	global_load_dwordx4 v[10:13], v1, s[0:1]
	global_load_dwordx4 v[14:17], v1, s[0:1] offset:16
	v_lshlrev_b32_e32 v1, 1, v0
	v_mov_b32_e32 v35, 0
	v_lshrrev_b32_e32 v18, 1, v0
	v_and_b32_e32 v34, 0x180, v1
	v_mov_b32_e32 v37, v35
	v_and_b32_e32 v36, 16, v18
	v_lshl_add_u64 v[18:19], s[6:7], 0, v[34:35]
	v_lshl_add_u64 v[38:39], v[18:19], 0, v[36:37]
	global_load_dwordx4 v[18:21], v[38:39], off
	global_load_dwordx4 v[22:25], v[38:39], off offset:32
	global_load_dwordx4 v[26:29], v[38:39], off offset:64
	global_load_dwordx4 v[30:33], v[38:39], off offset:96
	v_and_b32_e32 v0, 31, v0
	v_lshl_or_b32 v0, s2, 5, v0
	v_ashrrev_i32_e32 v1, 31, v0
	v_lshlrev_b64 v[0:1], 9, v[0:1]
	v_lshl_add_u64 v[0:1], s[8:9], 0, v[0:1]
	v_lshl_add_u64 v[0:1], v[0:1], 0, v[34:35]
	v_lshl_add_u64 v[34:35], v[0:1], 0, v[36:37]
	s_waitcnt vmcnt(7)
	v_cvt_f32_f16_e32 v0, v2
	v_cvt_f32_f16_sdwa v1, v2 dst_sel:DWORD dst_unused:UNUSED_PAD src0_sel:WORD_1
	v_cvt_f32_f16_e32 v2, v3
	v_cvt_f32_f16_sdwa v3, v3 dst_sel:DWORD dst_unused:UNUSED_PAD src0_sel:WORD_1
	v_cvt_f32_f16_e32 v36, v4
	v_cvt_f32_f16_sdwa v37, v4 dst_sel:DWORD dst_unused:UNUSED_PAD src0_sel:WORD_1
	s_waitcnt vmcnt(5)
	v_cvt_f32_f16_e32 v42, v10
	v_cvt_f32_f16_sdwa v43, v10 dst_sel:DWORD dst_unused:UNUSED_PAD src0_sel:WORD_1
	v_cvt_f32_f16_e32 v10, v11
	v_cvt_f32_f16_sdwa v11, v11 dst_sel:DWORD dst_unused:UNUSED_PAD src0_sel:WORD_1
	v_cvt_f32_f16_e32 v4, v5
	v_cvt_f32_f16_sdwa v5, v5 dst_sel:DWORD dst_unused:UNUSED_PAD src0_sel:WORD_1
	v_cvt_f32_f16_e32 v38, v6
	v_cvt_f32_f16_sdwa v39, v6 dst_sel:DWORD dst_unused:UNUSED_PAD src0_sel:WORD_1
	v_cvt_f32_f16_e32 v6, v7
	v_cvt_f32_f16_sdwa v7, v7 dst_sel:DWORD dst_unused:UNUSED_PAD src0_sel:WORD_1
	v_cvt_f32_f16_e32 v40, v8
	v_cvt_f32_f16_sdwa v41, v8 dst_sel:DWORD dst_unused:UNUSED_PAD src0_sel:WORD_1
	v_cvt_f32_f16_e32 v8, v9
	v_cvt_f32_f16_sdwa v9, v9 dst_sel:DWORD dst_unused:UNUSED_PAD src0_sel:WORD_1
	v_cvt_f32_f16_e32 v44, v12
	v_cvt_f32_f16_sdwa v45, v12 dst_sel:DWORD dst_unused:UNUSED_PAD src0_sel:WORD_1
	v_cvt_f32_f16_e32 v12, v13
	v_cvt_f32_f16_sdwa v13, v13 dst_sel:DWORD dst_unused:UNUSED_PAD src0_sel:WORD_1
	s_waitcnt vmcnt(4)
	v_cvt_f32_f16_e32 v46, v14
	v_cvt_f32_f16_sdwa v47, v14 dst_sel:DWORD dst_unused:UNUSED_PAD src0_sel:WORD_1
	v_cvt_f32_f16_e32 v14, v15
	v_cvt_f32_f16_sdwa v15, v15 dst_sel:DWORD dst_unused:UNUSED_PAD src0_sel:WORD_1
	v_cvt_f32_f16_e32 v48, v16
	v_cvt_f32_f16_sdwa v49, v16 dst_sel:DWORD dst_unused:UNUSED_PAD src0_sel:WORD_1
	v_cvt_f32_f16_e32 v16, v17
	v_cvt_f32_f16_sdwa v17, v17 dst_sel:DWORD dst_unused:UNUSED_PAD src0_sel:WORD_1
	v_pk_add_f32 v[0:1], v[0:1], v[42:43]
	v_pk_add_f32 v[2:3], v[2:3], v[10:11]
	v_pk_add_f32 v[10:11], v[36:37], v[44:45]
	v_pk_add_f32 v[12:13], v[4:5], v[12:13]
	v_pk_add_f32 v[36:37], v[38:39], v[46:47]
	v_pk_add_f32 v[14:15], v[6:7], v[14:15]
	v_pk_add_f32 v[38:39], v[40:41], v[48:49]
	v_pk_add_f32 v[16:17], v[8:9], v[16:17]
	s_waitcnt vmcnt(3)
	v_pk_add_f32 v[0:1], v[0:1], v[18:19]
	v_pk_add_f32 v[2:3], v[2:3], v[20:21]
	s_waitcnt vmcnt(2)
	v_pk_add_f32 v[4:5], v[10:11], v[22:23]
	v_pk_add_f32 v[6:7], v[12:13], v[24:25]
	s_waitcnt vmcnt(1)
	v_pk_add_f32 v[8:9], v[36:37], v[26:27]
	v_pk_add_f32 v[10:11], v[14:15], v[28:29]
	s_waitcnt vmcnt(0)
	v_pk_add_f32 v[12:13], v[38:39], v[30:31]
	v_pk_add_f32 v[14:15], v[16:17], v[32:33]
	global_store_dwordx4 v[34:35], v[0:3], off
	global_store_dwordx4 v[34:35], v[4:7], off offset:32
	global_store_dwordx4 v[34:35], v[8:11], off offset:64
	global_store_dwordx4 v[34:35], v[12:15], off offset:96
	s_endpgm

	.amdhsa_kernel _Z10fin_kernelPKfS0_Pf
		.amdhsa_group_segment_fixed_size 0
		.amdhsa_private_segment_fixed_size 0
		.amdhsa_kernarg_size 24
		.amdhsa_user_sgpr_count 2
		.amdhsa_user_sgpr_dispatch_ptr 0
		.amdhsa_user_sgpr_queue_ptr 0
		.amdhsa_user_sgpr_kernarg_segment_ptr 1
		.amdhsa_user_sgpr_dispatch_id 0
		.amdhsa_user_sgpr_kernarg_preload_length 0
		.amdhsa_user_sgpr_kernarg_preload_offset 0
		.amdhsa_user_sgpr_private_segment_size 0
		.amdhsa_uses_dynamic_stack 0
		.amdhsa_enable_private_segment 0
		.amdhsa_system_sgpr_workgroup_id_x 1
		.amdhsa_system_sgpr_workgroup_id_y 0
		.amdhsa_system_sgpr_workgroup_id_z 0
		.amdhsa_system_sgpr_workgroup_info 0
		.amdhsa_system_vgpr_workitem_id 0
		.amdhsa_next_free_vgpr 51
		.amdhsa_next_free_sgpr 12
		.amdhsa_accum_offset 52
		.amdhsa_reserve_vcc 0
		.amdhsa_float_round_mode_32 0
		.amdhsa_float_round_mode_16_64 0
		.amdhsa_float_denorm_mode_32 3
		.amdhsa_float_denorm_mode_16_64 3
		.amdhsa_dx10_clamp 1
		.amdhsa_ieee_mode 1
		.amdhsa_fp16_overflow 0
		.amdhsa_tg_split 0
		.amdhsa_exception_fp_ieee_invalid_op 0
		.amdhsa_exception_fp_denorm_src 0
		.amdhsa_exception_fp_ieee_div_zero 0
		.amdhsa_exception_fp_ieee_overflow 0
		.amdhsa_exception_fp_ieee_underflow 0
		.amdhsa_exception_fp_ieee_inexact 0
		.amdhsa_exception_int_div_zero 0
	.end_amdhsa_kernel

amdhsa.kernels:
  - .agpr_count:     0
    .args:
      - .actual_access:  read_only
        .address_space:  global
        .offset:         0
        .size:           8
        .value_kind:     global_buffer
      - .actual_access:  read_only
        .address_space:  global
        .offset:         8
        .size:           8
        .value_kind:     global_buffer
      - .actual_access:  read_only
        .address_space:  global
        .offset:         16
        .size:           8
        .value_kind:     global_buffer
      - .actual_access:  read_only
        .address_space:  global
        .offset:         24
        .size:           8
        .value_kind:     global_buffer
      - .actual_access:  read_only
        .address_space:  global
        .offset:         32
        .size:           8
        .value_kind:     global_buffer
      - .actual_access:  read_only
        .address_space:  global
        .offset:         40
        .size:           8
        .value_kind:     global_buffer
      - .address_space:  global
        .offset:         48
        .size:           8
        .value_kind:     global_buffer
      - .address_space:  global
        .offset:         56
        .size:           8
        .value_kind:     global_buffer
      - .address_space:  global
        .offset:         64
        .size:           8
        .value_kind:     global_buffer
      - .actual_access:  read_only
        .address_space:  global
        .offset:         72
        .size:           8
        .value_kind:     global_buffer
      - .actual_access:  read_only
        .address_space:  global
        .offset:         80
        .size:           8
        .value_kind:     global_buffer
      - .actual_access:  write_only
        .address_space:  global
        .offset:         88
        .size:           8
        .value_kind:     global_buffer
    .group_segment_fixed_size: 135456
    .kernarg_segment_align: 8
    .kernarg_segment_size: 96
    .language:       OpenCL C
    .language_version:
      - 2
      - 0
    .max_flat_workgroup_size: 512
    .name:           _Z11gram_kernelPKfPKiS0_S0_S0_S0_S0_S0_S0_S0_S0_Pf
    .private_segment_fixed_size: 0
    .sgpr_count:     66
    .sgpr_spill_count: 0
    .symbol:         _Z11gram_kernelPKfPKiS0_S0_S0_S0_S0_S0_S0_S0_S0_Pf.kd
    .uniform_work_group_size: 1
    .uses_dynamic_stack: false
    .vgpr_count:     252
    .vgpr_spill_count: 0
    .wavefront_size: 64
  - .agpr_count:     0
    .args:
      - .actual_access:  read_only
        .address_space:  global
        .offset:         0
        .size:           8
        .value_kind:     global_buffer
      - .actual_access:  read_only
        .address_space:  global
        .offset:         8
        .size:           8
        .value_kind:     global_buffer
      - .actual_access:  write_only
        .address_space:  global
        .offset:         16
        .size:           8
        .value_kind:     global_buffer
    .group_segment_fixed_size: 0
    .kernarg_segment_align: 8
    .kernarg_segment_size: 24
    .language:       OpenCL C
    .language_version:
      - 2
      - 0
    .max_flat_workgroup_size: 256
    .name:           _Z10fin_kernelPKfS0_Pf
    .private_segment_fixed_size: 0
    .sgpr_count:     16
    .sgpr_spill_count: 0
    .symbol:         _Z10fin_kernelPKfS0_Pf.kd
    .uniform_work_group_size: 1
    .uses_dynamic_stack: false
    .vgpr_count:     51
    .vgpr_spill_count: 0
    .wavefront_size: 64
